# biaspk
# speedup vs baseline: 1.0049x; 1.0049x over previous
_Z11prep_kernelPKfS0_S0_S0_S0_S0_S0_S0_PhPf:
	s_load_dwordx2 s[6:7], s[0:1], 0x40
	s_load_dwordx2 s[8:9], s[0:1], 0x8
	s_cmp_gt_u32 s2, 21
	s_mov_b64 s[4:5], -1
	s_cbranch_scc0 .LBB0_43
	s_cmpk_lt_u32 s2, 0x216
	s_cbranch_scc0 .LBB0_23
	v_and_b32_e32 v1, 0x7f, v0
	v_mov_b32_e32 v3, 0
	v_lshlrev_b32_e32 v2, 2, v1
	s_waitcnt lgkmcnt(0)
	v_lshl_add_u64 v[4:5], s[8:9], 0, v[2:3]
	v_add_co_u32_e32 v6, vcc, 0x3000, v4
	v_lshlrev_b32_e32 v1, 2, v0
	s_nop 0
	v_addc_co_u32_e32 v7, vcc, 0, v5, vcc
	v_add_co_u32_e32 v8, vcc, 0x2c000, v4
	v_or_b32_e32 v3, 0x2ce00, v1
	s_nop 0
	v_addc_co_u32_e32 v9, vcc, 0, v5, vcc
	global_load_dword v41, v[6:7], off offset:1536
	global_load_dword v39, v[6:7], off offset:2048
	global_load_dword v37, v[6:7], off offset:2560
	global_load_dword v36, v[8:9], off offset:1024
	global_load_dword v35, v[8:9], off offset:1536
	global_load_dword v34, v[8:9], off offset:2048
	global_load_dword v33, v[8:9], off offset:2560
	global_load_dword v32, v[8:9], off offset:3072
	v_add_co_u32_e32 v6, vcc, 0x2d000, v4
	s_load_dwordx2 s[4:5], s[0:1], 0x10
	s_nop 0
	v_addc_co_u32_e32 v7, vcc, 0, v5, vcc
	global_load_dword v42, v3, s[8:9]
	global_load_dword v44, v[6:7], off
	global_load_dword v43, v[6:7], off offset:512
	global_load_dword v40, v[6:7], off offset:1024
	global_load_dword v38, v[6:7], off offset:1536
	global_load_dword v26, v[6:7], off offset:2048
	global_load_dword v27, v[6:7], off offset:2560
	global_load_dword v28, v[6:7], off offset:3072
	v_add_co_u32_e32 v6, vcc, 0x2e000, v4
	v_or_b32_e32 v3, 0x2de00, v1
	s_nop 0
	v_addc_co_u32_e32 v7, vcc, 0, v5, vcc
	global_load_dword v24, v3, s[8:9]
	global_load_dword v29, v[6:7], off
	global_load_dword v30, v[6:7], off offset:512
	global_load_dword v31, v[6:7], off offset:1024
	global_load_dword v25, v[6:7], off offset:1536
	global_load_dword v18, v[6:7], off offset:2048
	global_load_dword v19, v[6:7], off offset:2560
	global_load_dword v20, v[6:7], off offset:3072
	v_add_co_u32_e32 v6, vcc, 0x2f000, v4
	v_or_b32_e32 v3, 0x2ee00, v1
	s_nop 0
	v_addc_co_u32_e32 v7, vcc, 0, v5, vcc
	global_load_dword v16, v3, s[8:9]
	global_load_dword v21, v[6:7], off
	global_load_dword v22, v[6:7], off offset:512
	global_load_dword v23, v[6:7], off offset:1024
	global_load_dword v17, v[6:7], off offset:1536
	global_load_dword v10, v[6:7], off offset:2048
	global_load_dword v11, v[6:7], off offset:2560
	global_load_dword v12, v[6:7], off offset:3072
	v_or_b32_e32 v3, 0x2fe00, v1
	v_add_co_u32_e32 v4, vcc, 0x30000, v4
	s_lshl_b32 s3, s2, 3
	s_nop 0
	v_addc_co_u32_e32 v5, vcc, 0, v5, vcc
	global_load_dword v7, v3, s[8:9]
	global_load_dword v13, v[4:5], off
	global_load_dword v14, v[4:5], off offset:512
	global_load_dword v15, v[4:5], off offset:1024
	global_load_dword v9, v[4:5], off offset:1536
	global_load_dword v8, v[4:5], off offset:2048
	global_load_dword v6, v[4:5], off offset:2560
	s_waitcnt lgkmcnt(0)
	global_load_dword v1, v2, s[4:5]
	s_load_dwordx2 s[4:5], s[0:1], 0x0
	s_addk_i32 s3, 0xff50
	v_or_b32_e32 v3, 0x100, v0
	v_mul_u32_u24_e32 v46, 0x691, v0
	v_mul_u32_u24_e32 v55, 0x691, v3
	v_lshrrev_b32_e32 v46, 16, v46
	v_lshrrev_b32_e32 v55, 16, v55
	v_mul_u32_u24_e32 v4, 39, v46
	v_mul_u32_u24_e32 v5, 39, v55
	v_sub_u32_e32 v45, v0, v4
	v_sub_u32_e32 v54, v3, v5
	v_cmp_gt_u32_e32 vcc, 21, v45
	v_add_u32_e32 v4, -3, v45
	v_add_u32_e32 v5, -21, v45
	s_mov_b64 s[12:13], vcc
	v_cndmask_b32_e32 v47, v5, v4, vcc
	v_cmp_gt_u32_e32 vcc, 3, v45
	v_mul_u32_u24_e32 v48, 43, v47
	v_lshrrev_b32_e32 v48, 8, v48
	s_mov_b64 s[14:15], vcc
	v_mul_u32_u24_e32 v4, 6, v48
	v_sub_u32_e32 v49, v47, v4
	v_cndmask_b32_e32 v48, v48, v45, vcc
	v_add_u32_e32 v50, s3, v46
	v_lshl_add_u32 v50, v50, 1, v50
	v_add_u32_e32 v50, v50, v48
	v_lshlrev_b32_e32 v50, 2, v50
	v_lshlrev_b32_e64 v51, v49, 1
	v_cvt_f32_u32_e32 v51, v51
	v_mul_f32_e32 v51, 0.15915494, v51
	v_lshlrev_b32_e32 v53, 2, v46
	v_lshl_add_u32 v53, v45, 5, v53
	v_cmp_gt_u32_e32 vcc, 21, v54
	v_add_u32_e32 v4, -3, v54
	v_add_u32_e32 v5, -21, v54
	s_mov_b64 s[16:17], vcc
	v_cndmask_b32_e32 v56, v5, v4, vcc
	v_cmp_gt_u32_e32 vcc, 3, v54
	v_mul_u32_u24_e32 v57, 43, v56
	v_lshrrev_b32_e32 v57, 8, v57
	s_mov_b64 s[18:19], vcc
	v_mul_u32_u24_e32 v4, 6, v57
	v_sub_u32_e32 v58, v56, v4
	v_cndmask_b32_e32 v57, v57, v54, vcc
	v_add_u32_e32 v59, s3, v55
	v_lshl_add_u32 v59, v59, 1, v59
	v_add_u32_e32 v59, v59, v57
	v_lshlrev_b32_e32 v59, 2, v59
	v_lshlrev_b32_e64 v60, v58, 1
	v_cvt_f32_u32_e32 v60, v60
	v_mul_f32_e32 v60, 0.15915494, v60
	v_lshlrev_b32_e32 v62, 2, v55
	v_lshl_add_u32 v62, v54, 5, v62
	s_waitcnt lgkmcnt(0)
	global_load_dword v52, v50, s[4:5]
	v_cmp_gt_u32_e32 vcc, 56, v0
	s_and_saveexec_b64 s[10:11], vcc
	s_cbranch_execz .Lenc_skip1
	global_load_dword v61, v59, s[4:5]

.Lenc_skip2:
	s_or_b64 exec, exec, s[10:11]
	v_lshrrev_b32_e32 v45, 5, v0
	v_and_b32_e32 v54, 4, v45
	v_lshlrev_b32_e32 v45, 2, v54
	s_waitcnt vmcnt(0) lgkmcnt(0)
	s_barrier
	ds_read_b128 v[50:53], v45
	v_mov_b32_e32 v46, v1
	v_mov_b32_e32 v47, v1
	v_mov_b32_e32 v48, v1
	v_mov_b32_e32 v49, v1
	v_add_u32_e32 v3, s3, v54
	v_lshlrev_b32_e32 v3, 9, v3
	v_add_u32_e32 v3, v3, v2
	v_add_u32_e32 v3, 0x16000, v3
	ds_read_b128 v[56:59], v45 offset:32
	s_waitcnt lgkmcnt(1)
	v_pk_fma_f32 v[46:47], v[50:51], v[40:41], v[46:47] op_sel:[0,1,0] op_sel_hi:[1,1,1]
	v_pk_fma_f32 v[48:49], v[52:53], v[40:41], v[48:49] op_sel:[0,1,0] op_sel_hi:[1,1,1]
	ds_read_b128 v[50:53], v45 offset:64
	s_waitcnt lgkmcnt(1)
	v_pk_fma_f32 v[46:47], v[56:57], v[38:39], v[46:47] op_sel:[0,1,0] op_sel_hi:[1,1,1]
	v_pk_fma_f32 v[48:49], v[58:59], v[38:39], v[48:49] op_sel:[0,1,0] op_sel_hi:[1,1,1]
	ds_read_b128 v[56:59], v45 offset:96
	s_waitcnt lgkmcnt(1)
	v_pk_fma_f32 v[46:47], v[50:51], v[36:37], v[46:47] op_sel:[0,1,0] op_sel_hi:[1,1,1]
	v_pk_fma_f32 v[48:49], v[52:53], v[36:37], v[48:49] op_sel:[0,1,0] op_sel_hi:[1,1,1]
	ds_read_b128 v[50:53], v45 offset:128
	s_waitcnt lgkmcnt(1)
	v_pk_fma_f32 v[46:47], v[56:57], v[36:37], v[46:47] op_sel_hi:[1,0,1]
	v_pk_fma_f32 v[48:49], v[58:59], v[36:37], v[48:49] op_sel_hi:[1,0,1]
	ds_read_b128 v[56:59], v45 offset:160
	s_waitcnt lgkmcnt(1)
	v_pk_fma_f32 v[46:47], v[50:51], v[34:35], v[46:47] op_sel:[0,1,0] op_sel_hi:[1,1,1]
	v_pk_fma_f32 v[48:49], v[52:53], v[34:35], v[48:49] op_sel:[0,1,0] op_sel_hi:[1,1,1]
	ds_read_b128 v[50:53], v45 offset:192
	s_waitcnt lgkmcnt(1)
	v_pk_fma_f32 v[46:47], v[56:57], v[34:35], v[46:47] op_sel_hi:[1,0,1]
	v_pk_fma_f32 v[48:49], v[58:59], v[34:35], v[48:49] op_sel_hi:[1,0,1]
	ds_read_b128 v[56:59], v45 offset:224
	s_waitcnt lgkmcnt(1)
	v_pk_fma_f32 v[46:47], v[50:51], v[32:33], v[46:47] op_sel:[0,1,0] op_sel_hi:[1,1,1]
	v_pk_fma_f32 v[48:49], v[52:53], v[32:33], v[48:49] op_sel:[0,1,0] op_sel_hi:[1,1,1]
	ds_read_b128 v[50:53], v45 offset:256
	s_waitcnt lgkmcnt(1)
	v_pk_fma_f32 v[46:47], v[56:57], v[32:33], v[46:47] op_sel_hi:[1,0,1]
	v_pk_fma_f32 v[48:49], v[58:59], v[32:33], v[48:49] op_sel_hi:[1,0,1]
	ds_read_b128 v[56:59], v45 offset:288
	s_waitcnt lgkmcnt(1)
	v_pk_fma_f32 v[46:47], v[50:51], v[42:43], v[46:47] op_sel_hi:[1,0,1]
	v_pk_fma_f32 v[48:49], v[52:53], v[42:43], v[48:49] op_sel_hi:[1,0,1]
	ds_read_b128 v[50:53], v45 offset:320
	s_waitcnt lgkmcnt(1)
	v_pk_fma_f32 v[46:47], v[56:57], v[44:45], v[46:47] op_sel_hi:[1,0,1]
	v_pk_fma_f32 v[48:49], v[58:59], v[44:45], v[48:49] op_sel_hi:[1,0,1]
	ds_read_b128 v[56:59], v45 offset:352
	s_waitcnt lgkmcnt(1)
	v_pk_fma_f32 v[46:47], v[50:51], v[42:43], v[46:47] op_sel:[0,1,0] op_sel_hi:[1,1,1]
	v_pk_fma_f32 v[48:49], v[52:53], v[42:43], v[48:49] op_sel:[0,1,0] op_sel_hi:[1,1,1]
	ds_read_b128 v[50:53], v45 offset:384
	s_waitcnt lgkmcnt(1)
	v_pk_fma_f32 v[46:47], v[56:57], v[40:41], v[46:47] op_sel_hi:[1,0,1]
	v_pk_fma_f32 v[48:49], v[58:59], v[40:41], v[48:49] op_sel_hi:[1,0,1]
	ds_read_b128 v[56:59], v45 offset:416
	s_waitcnt lgkmcnt(1)
	v_pk_fma_f32 v[46:47], v[50:51], v[38:39], v[46:47] op_sel_hi:[1,0,1]
	v_pk_fma_f32 v[48:49], v[52:53], v[38:39], v[48:49] op_sel_hi:[1,0,1]
	ds_read_b128 v[50:53], v45 offset:448
	s_waitcnt lgkmcnt(1)
	v_pk_fma_f32 v[46:47], v[56:57], v[26:27], v[46:47] op_sel_hi:[1,0,1]
	v_pk_fma_f32 v[48:49], v[58:59], v[26:27], v[48:49] op_sel_hi:[1,0,1]
	ds_read_b128 v[56:59], v45 offset:480
	s_waitcnt lgkmcnt(1)
	v_pk_fma_f32 v[46:47], v[50:51], v[26:27], v[46:47] op_sel:[0,1,0] op_sel_hi:[1,1,1]
	v_pk_fma_f32 v[48:49], v[52:53], v[26:27], v[48:49] op_sel:[0,1,0] op_sel_hi:[1,1,1]
	ds_read_b128 v[50:53], v45 offset:512
	s_waitcnt lgkmcnt(1)
	v_pk_fma_f32 v[46:47], v[56:57], v[28:29], v[46:47] op_sel_hi:[1,0,1]
	v_pk_fma_f32 v[48:49], v[58:59], v[28:29], v[48:49] op_sel_hi:[1,0,1]
	ds_read_b128 v[56:59], v45 offset:544
	s_waitcnt lgkmcnt(1)
	v_pk_fma_f32 v[46:47], v[50:51], v[24:25], v[46:47] op_sel_hi:[1,0,1]
	v_pk_fma_f32 v[48:49], v[52:53], v[24:25], v[48:49] op_sel_hi:[1,0,1]
	ds_read_b128 v[50:53], v45 offset:576
	s_waitcnt lgkmcnt(1)
	v_pk_fma_f32 v[46:47], v[56:57], v[28:29], v[46:47] op_sel:[0,1,0] op_sel_hi:[1,1,1]
	v_pk_fma_f32 v[48:49], v[58:59], v[28:29], v[48:49] op_sel:[0,1,0] op_sel_hi:[1,1,1]
	ds_read_b128 v[56:59], v45 offset:608
	s_waitcnt lgkmcnt(1)
	v_pk_fma_f32 v[46:47], v[50:51], v[30:31], v[46:47] op_sel_hi:[1,0,1]
	v_pk_fma_f32 v[48:49], v[52:53], v[30:31], v[48:49] op_sel_hi:[1,0,1]
	ds_read_b128 v[50:53], v45 offset:640
	s_waitcnt lgkmcnt(1)
	v_pk_fma_f32 v[46:47], v[56:57], v[30:31], v[46:47] op_sel:[0,1,0] op_sel_hi:[1,1,1]
	v_pk_fma_f32 v[48:49], v[58:59], v[30:31], v[48:49] op_sel:[0,1,0] op_sel_hi:[1,1,1]
	ds_read_b128 v[56:59], v45 offset:672
	s_waitcnt lgkmcnt(1)
	v_pk_fma_f32 v[46:47], v[50:51], v[24:25], v[46:47] op_sel:[0,1,0] op_sel_hi:[1,1,1]
	v_pk_fma_f32 v[48:49], v[52:53], v[24:25], v[48:49] op_sel:[0,1,0] op_sel_hi:[1,1,1]
	ds_read_b128 v[50:53], v45 offset:704
	s_waitcnt lgkmcnt(1)
	v_pk_fma_f32 v[46:47], v[56:57], v[18:19], v[46:47] op_sel_hi:[1,0,1]
	v_pk_fma_f32 v[48:49], v[58:59], v[18:19], v[48:49] op_sel_hi:[1,0,1]
	ds_read_b128 v[56:59], v45 offset:736
	s_waitcnt lgkmcnt(1)
	v_pk_fma_f32 v[46:47], v[50:51], v[18:19], v[46:47] op_sel:[0,1,0] op_sel_hi:[1,1,1]
	v_pk_fma_f32 v[48:49], v[52:53], v[18:19], v[48:49] op_sel:[0,1,0] op_sel_hi:[1,1,1]
	ds_read_b128 v[50:53], v45 offset:768
	s_waitcnt lgkmcnt(1)
	v_pk_fma_f32 v[46:47], v[56:57], v[20:21], v[46:47] op_sel_hi:[1,0,1]
	v_pk_fma_f32 v[48:49], v[58:59], v[20:21], v[48:49] op_sel_hi:[1,0,1]
	ds_read_b128 v[56:59], v45 offset:800
	s_waitcnt lgkmcnt(1)
	v_pk_fma_f32 v[46:47], v[50:51], v[16:17], v[46:47] op_sel_hi:[1,0,1]
	v_pk_fma_f32 v[48:49], v[52:53], v[16:17], v[48:49] op_sel_hi:[1,0,1]
	ds_read_b128 v[50:53], v45 offset:832
	s_waitcnt lgkmcnt(1)
	v_pk_fma_f32 v[46:47], v[56:57], v[20:21], v[46:47] op_sel:[0,1,0] op_sel_hi:[1,1,1]
	v_pk_fma_f32 v[48:49], v[58:59], v[20:21], v[48:49] op_sel:[0,1,0] op_sel_hi:[1,1,1]
	ds_read_b128 v[56:59], v45 offset:864
	s_waitcnt lgkmcnt(1)
	v_pk_fma_f32 v[46:47], v[50:51], v[22:23], v[46:47] op_sel_hi:[1,0,1]
	v_pk_fma_f32 v[48:49], v[52:53], v[22:23], v[48:49] op_sel_hi:[1,0,1]
	ds_read_b128 v[50:53], v45 offset:896
	s_waitcnt lgkmcnt(1)
	v_pk_fma_f32 v[46:47], v[56:57], v[22:23], v[46:47] op_sel:[0,1,0] op_sel_hi:[1,1,1]
	v_pk_fma_f32 v[48:49], v[58:59], v[22:23], v[48:49] op_sel:[0,1,0] op_sel_hi:[1,1,1]
	ds_read_b128 v[56:59], v45 offset:928
	s_waitcnt lgkmcnt(1)
	v_pk_fma_f32 v[46:47], v[50:51], v[16:17], v[46:47] op_sel:[0,1,0] op_sel_hi:[1,1,1]
	v_pk_fma_f32 v[48:49], v[52:53], v[16:17], v[48:49] op_sel:[0,1,0] op_sel_hi:[1,1,1]
	ds_read_b128 v[50:53], v45 offset:960
	s_waitcnt lgkmcnt(1)
	v_pk_fma_f32 v[46:47], v[56:57], v[10:11], v[46:47] op_sel_hi:[1,0,1]
	v_pk_fma_f32 v[48:49], v[58:59], v[10:11], v[48:49] op_sel_hi:[1,0,1]
	ds_read_b128 v[56:59], v45 offset:992
	s_waitcnt lgkmcnt(1)
	v_pk_fma_f32 v[46:47], v[50:51], v[10:11], v[46:47] op_sel:[0,1,0] op_sel_hi:[1,1,1]
	v_pk_fma_f32 v[48:49], v[52:53], v[10:11], v[48:49] op_sel:[0,1,0] op_sel_hi:[1,1,1]
	ds_read_b128 v[50:53], v45 offset:1024
	s_waitcnt lgkmcnt(1)
	v_pk_fma_f32 v[46:47], v[56:57], v[12:13], v[46:47] op_sel_hi:[1,0,1]
	v_pk_fma_f32 v[48:49], v[58:59], v[12:13], v[48:49] op_sel_hi:[1,0,1]
	ds_read_b128 v[56:59], v45 offset:1056
	s_waitcnt lgkmcnt(1)
	v_pk_fma_f32 v[46:47], v[50:51], v[6:7], v[46:47] op_sel:[0,1,0] op_sel_hi:[1,1,1]
	v_pk_fma_f32 v[48:49], v[52:53], v[6:7], v[48:49] op_sel:[0,1,0] op_sel_hi:[1,1,1]
	ds_read_b128 v[50:53], v45 offset:1088
	s_waitcnt lgkmcnt(1)
	v_pk_fma_f32 v[46:47], v[56:57], v[12:13], v[46:47] op_sel:[0,1,0] op_sel_hi:[1,1,1]
	v_pk_fma_f32 v[48:49], v[58:59], v[12:13], v[48:49] op_sel:[0,1,0] op_sel_hi:[1,1,1]
	ds_read_b128 v[56:59], v45 offset:1120
	s_waitcnt lgkmcnt(1)
	v_pk_fma_f32 v[46:47], v[50:51], v[14:15], v[46:47] op_sel_hi:[1,0,1]
	v_pk_fma_f32 v[48:49], v[52:53], v[14:15], v[48:49] op_sel_hi:[1,0,1]
	ds_read_b128 v[50:53], v45 offset:1152
	s_waitcnt lgkmcnt(1)
	v_pk_fma_f32 v[46:47], v[56:57], v[14:15], v[46:47] op_sel:[0,1,0] op_sel_hi:[1,1,1]
	v_pk_fma_f32 v[48:49], v[58:59], v[14:15], v[48:49] op_sel:[0,1,0] op_sel_hi:[1,1,1]
	ds_read_b128 v[56:59], v45 offset:1184
	s_waitcnt lgkmcnt(1)
	v_pk_fma_f32 v[46:47], v[50:51], v[8:9], v[46:47] op_sel:[0,1,0] op_sel_hi:[1,1,1]
	v_pk_fma_f32 v[48:49], v[52:53], v[8:9], v[48:49] op_sel:[0,1,0] op_sel_hi:[1,1,1]
	ds_read_b128 v[50:53], v45 offset:1216
	s_waitcnt lgkmcnt(1)
	v_pk_fma_f32 v[46:47], v[56:57], v[8:9], v[46:47] op_sel_hi:[1,0,1]
	v_pk_fma_f32 v[48:49], v[58:59], v[8:9], v[48:49] op_sel_hi:[1,0,1]
	s_waitcnt lgkmcnt(0)
	v_pk_fma_f32 v[46:47], v[50:51], v[6:7], v[46:47] op_sel_hi:[1,0,1]
	v_pk_fma_f32 v[48:49], v[52:53], v[6:7], v[48:49] op_sel_hi:[1,0,1]
	v_mul_f32_e32 v46, 0xf800000, v46
	v_mul_f32_e32 v47, 0xf800000, v47
	v_mul_f32_e32 v48, 0xf800000, v48
	v_mul_f32_e32 v49, 0xf800000, v49
	global_store_dword v3, v46, s[6:7] offset:0
	global_store_dword v3, v47, s[6:7] offset:512
	global_store_dword v3, v48, s[6:7] offset:1024
	global_store_dword v3, v49, s[6:7] offset:1536
	s_mov_b64 s[4:5], 0
